# accumulator zeroing ahead of each GEMM K-loop with 64-bit moves (64 v_mov_b64 instead of 127 v_mov_b32) in all 8 GEMMs
# speedup vs baseline: 1.0053x; 1.0036x over previous
.LBB0_1221:
	s_andn2_b64 vcc, exec, s[10:11]
	s_cbranch_vccnz .LBB0_1237
	s_add_u32 s68, s44, 0x100
	s_addc_u32 s69, s45, 0
	s_add_u32 s70, s42, 0x100
	s_addc_u32 s71, s43, 0
	s_add_u32 s72, s38, 0x100
	s_addc_u32 s73, s39, 0
	s_add_u32 s74, s40, 0x100
	v_mov_b32_e32 v0, 0
	s_addc_u32 s75, s41, 0
	s_mov_b32 s38, 0
	v_mov_b64_e32 v[0:1], 0
	v_mov_b64_e32 v[2:3], 0
	v_mov_b64_e32 v[4:5], 0
	v_mov_b64_e32 v[6:7], 0
	v_mov_b64_e32 v[8:9], 0
	v_mov_b64_e32 v[10:11], 0
	v_mov_b64_e32 v[12:13], 0
	v_mov_b64_e32 v[14:15], 0
	v_mov_b64_e32 v[16:17], 0
	v_mov_b64_e32 v[18:19], 0
	v_mov_b64_e32 v[20:21], 0
	v_mov_b64_e32 v[22:23], 0
	v_mov_b64_e32 v[24:25], 0
	v_mov_b64_e32 v[26:27], 0
	v_mov_b64_e32 v[28:29], 0
	v_mov_b64_e32 v[30:31], 0
	v_mov_b64_e32 v[32:33], 0
	v_mov_b64_e32 v[34:35], 0
	v_mov_b64_e32 v[36:37], 0
	v_mov_b64_e32 v[38:39], 0
	v_mov_b64_e32 v[40:41], 0
	v_mov_b64_e32 v[42:43], 0
	v_mov_b64_e32 v[44:45], 0
	v_mov_b64_e32 v[46:47], 0
	v_mov_b64_e32 v[48:49], 0
	v_mov_b64_e32 v[50:51], 0
	v_mov_b64_e32 v[52:53], 0
	v_mov_b64_e32 v[54:55], 0
	v_mov_b64_e32 v[56:57], 0
	v_mov_b64_e32 v[58:59], 0
	v_mov_b64_e32 v[60:61], 0
	v_mov_b64_e32 v[62:63], 0
	v_mov_b64_e32 v[64:65], 0
	v_mov_b64_e32 v[66:67], 0
	v_mov_b64_e32 v[68:69], 0
	v_mov_b64_e32 v[70:71], 0
	v_mov_b64_e32 v[72:73], 0
	v_mov_b64_e32 v[74:75], 0
	v_mov_b64_e32 v[76:77], 0
	v_mov_b64_e32 v[78:79], 0
	v_mov_b64_e32 v[80:81], 0
	v_mov_b64_e32 v[82:83], 0
	v_mov_b64_e32 v[84:85], 0
	v_mov_b64_e32 v[86:87], 0
	v_mov_b64_e32 v[88:89], 0
	v_mov_b64_e32 v[90:91], 0
	v_mov_b64_e32 v[92:93], 0
	v_mov_b64_e32 v[94:95], 0
	v_mov_b64_e32 v[96:97], 0
	v_mov_b64_e32 v[98:99], 0
	v_mov_b64_e32 v[100:101], 0
	v_mov_b64_e32 v[102:103], 0
	v_mov_b64_e32 v[104:105], 0
	v_mov_b64_e32 v[106:107], 0
	v_mov_b64_e32 v[108:109], 0
	v_mov_b64_e32 v[110:111], 0
	v_mov_b64_e32 v[112:113], 0
	v_mov_b64_e32 v[114:115], 0
	v_mov_b64_e32 v[116:117], 0
	v_mov_b64_e32 v[118:119], 0
	v_mov_b64_e32 v[120:121], 0
	v_mov_b64_e32 v[122:123], 0
	v_mov_b64_e32 v[124:125], 0
	v_mov_b64_e32 v[126:127], 0

.LBB0_1250:
	s_andn2_b64 vcc, exec, s[10:11]
	s_cbranch_vccnz .LBB0_1258
	s_add_u32 s65, s44, 0x100
	s_addc_u32 s66, s45, 0
	s_add_u32 s67, s42, 0x100
	s_addc_u32 s68, s43, 0
	s_add_u32 s69, s38, 0x100
	s_addc_u32 s70, s39, 0
	s_add_u32 s71, s40, 0x100
	v_mov_b32_e32 v0, 0
	s_addc_u32 s72, s41, 0
	s_mov_b32 s38, 0
	v_mov_b64_e32 v[0:1], 0
	v_mov_b64_e32 v[2:3], 0
	v_mov_b64_e32 v[4:5], 0
	v_mov_b64_e32 v[6:7], 0
	v_mov_b64_e32 v[8:9], 0
	v_mov_b64_e32 v[10:11], 0
	v_mov_b64_e32 v[12:13], 0
	v_mov_b64_e32 v[14:15], 0
	v_mov_b64_e32 v[16:17], 0
	v_mov_b64_e32 v[18:19], 0
	v_mov_b64_e32 v[20:21], 0
	v_mov_b64_e32 v[22:23], 0
	v_mov_b64_e32 v[24:25], 0
	v_mov_b64_e32 v[26:27], 0
	v_mov_b64_e32 v[28:29], 0
	v_mov_b64_e32 v[30:31], 0
	v_mov_b64_e32 v[32:33], 0
	v_mov_b64_e32 v[34:35], 0
	v_mov_b64_e32 v[36:37], 0
	v_mov_b64_e32 v[38:39], 0
	v_mov_b64_e32 v[40:41], 0
	v_mov_b64_e32 v[42:43], 0
	v_mov_b64_e32 v[44:45], 0
	v_mov_b64_e32 v[46:47], 0
	v_mov_b64_e32 v[48:49], 0
	v_mov_b64_e32 v[50:51], 0
	v_mov_b64_e32 v[52:53], 0
	v_mov_b64_e32 v[54:55], 0
	v_mov_b64_e32 v[56:57], 0
	v_mov_b64_e32 v[58:59], 0
	v_mov_b64_e32 v[60:61], 0
	v_mov_b64_e32 v[62:63], 0
	v_mov_b64_e32 v[64:65], 0
	v_mov_b64_e32 v[66:67], 0
	v_mov_b64_e32 v[68:69], 0
	v_mov_b64_e32 v[70:71], 0
	v_mov_b64_e32 v[72:73], 0
	v_mov_b64_e32 v[74:75], 0
	v_mov_b64_e32 v[76:77], 0
	v_mov_b64_e32 v[78:79], 0
	v_mov_b64_e32 v[80:81], 0
	v_mov_b64_e32 v[82:83], 0
	v_mov_b64_e32 v[84:85], 0
	v_mov_b64_e32 v[86:87], 0
	v_mov_b64_e32 v[88:89], 0
	v_mov_b64_e32 v[90:91], 0
	v_mov_b64_e32 v[92:93], 0
	v_mov_b64_e32 v[94:95], 0
	v_mov_b64_e32 v[96:97], 0
	v_mov_b64_e32 v[98:99], 0
	v_mov_b64_e32 v[100:101], 0
	v_mov_b64_e32 v[102:103], 0
	v_mov_b64_e32 v[104:105], 0
	v_mov_b64_e32 v[106:107], 0
	v_mov_b64_e32 v[108:109], 0
	v_mov_b64_e32 v[110:111], 0
	v_mov_b64_e32 v[112:113], 0
	v_mov_b64_e32 v[114:115], 0
	v_mov_b64_e32 v[116:117], 0
	v_mov_b64_e32 v[118:119], 0
	v_mov_b64_e32 v[120:121], 0
	v_mov_b64_e32 v[122:123], 0
	v_mov_b64_e32 v[124:125], 0
	v_mov_b64_e32 v[126:127], 0

.LBB0_1279:
	s_andn2_b64 vcc, exec, s[16:17]
	s_cbranch_vccnz .LBB0_1287
	s_add_u32 s78, s56, 0x100
	s_addc_u32 s79, s57, 0
	s_add_u32 s80, s54, 0x100
	s_addc_u32 s81, s55, 0
	s_add_u32 s82, s52, 0x100
	s_addc_u32 s83, s53, 0
	s_add_u32 s84, s58, 0x100
	v_mov_b32_e32 v0, 0
	s_addc_u32 s85, s59, 0
	s_mov_b32 s52, 0
	v_mov_b64_e32 v[0:1], 0
	v_mov_b64_e32 v[2:3], 0
	v_mov_b64_e32 v[4:5], 0
	v_mov_b64_e32 v[6:7], 0
	v_mov_b64_e32 v[8:9], 0
	v_mov_b64_e32 v[10:11], 0
	v_mov_b64_e32 v[12:13], 0
	v_mov_b64_e32 v[14:15], 0
	v_mov_b64_e32 v[16:17], 0
	v_mov_b64_e32 v[18:19], 0
	v_mov_b64_e32 v[20:21], 0
	v_mov_b64_e32 v[22:23], 0
	v_mov_b64_e32 v[24:25], 0
	v_mov_b64_e32 v[26:27], 0
	v_mov_b64_e32 v[28:29], 0
	v_mov_b64_e32 v[30:31], 0
	v_mov_b64_e32 v[32:33], 0
	v_mov_b64_e32 v[34:35], 0
	v_mov_b64_e32 v[36:37], 0
	v_mov_b64_e32 v[38:39], 0
	v_mov_b64_e32 v[40:41], 0
	v_mov_b64_e32 v[42:43], 0
	v_mov_b64_e32 v[44:45], 0
	v_mov_b64_e32 v[46:47], 0
	v_mov_b64_e32 v[48:49], 0
	v_mov_b64_e32 v[50:51], 0
	v_mov_b64_e32 v[52:53], 0
	v_mov_b64_e32 v[54:55], 0
	v_mov_b64_e32 v[56:57], 0
	v_mov_b64_e32 v[58:59], 0
	v_mov_b64_e32 v[60:61], 0
	v_mov_b64_e32 v[62:63], 0
	v_mov_b64_e32 v[64:65], 0
	v_mov_b64_e32 v[66:67], 0
	v_mov_b64_e32 v[68:69], 0
	v_mov_b64_e32 v[70:71], 0
	v_mov_b64_e32 v[72:73], 0
	v_mov_b64_e32 v[74:75], 0
	v_mov_b64_e32 v[76:77], 0
	v_mov_b64_e32 v[78:79], 0
	v_mov_b64_e32 v[80:81], 0
	v_mov_b64_e32 v[82:83], 0
	v_mov_b64_e32 v[84:85], 0
	v_mov_b64_e32 v[86:87], 0
	v_mov_b64_e32 v[88:89], 0
	v_mov_b64_e32 v[90:91], 0
	v_mov_b64_e32 v[92:93], 0
	v_mov_b64_e32 v[94:95], 0
	v_mov_b64_e32 v[100:101], 0
	v_mov_b64_e32 v[102:103], 0
	v_mov_b64_e32 v[104:105], 0
	v_mov_b64_e32 v[106:107], 0
	v_mov_b64_e32 v[108:109], 0
	v_mov_b64_e32 v[110:111], 0
	v_mov_b64_e32 v[112:113], 0
	v_mov_b64_e32 v[114:115], 0
	v_mov_b64_e32 v[120:121], 0
	v_mov_b64_e32 v[122:123], 0
	v_mov_b64_e32 v[124:125], 0
	v_mov_b64_e32 v[126:127], 0
	v_mov_b64_e32 v[128:129], 0
	v_mov_b64_e32 v[130:131], 0
	v_mov_b64_e32 v[132:133], 0
	v_mov_b64_e32 v[134:135], 0

.LBB0_1432:
	s_andn2_b64 vcc, exec, s[22:23]
	s_cbranch_vccnz .LBB0_1458
	s_add_u32 s78, s50, 0x100
	s_addc_u32 s79, s51, 0
	s_add_u32 s80, s48, 0x100
	s_addc_u32 s81, s49, 0
	s_add_u32 s82, s12, 0x100
	s_addc_u32 s83, s13, 0
	s_add_u32 s84, s52, 0x100
	v_mov_b32_e32 v0, 0
	s_addc_u32 s85, s53, 0
	s_mov_b32 s12, 0
	v_mov_b64_e32 v[0:1], 0
	v_mov_b64_e32 v[2:3], 0
	v_mov_b64_e32 v[4:5], 0
	v_mov_b64_e32 v[6:7], 0
	v_mov_b64_e32 v[8:9], 0
	v_mov_b64_e32 v[10:11], 0
	v_mov_b64_e32 v[12:13], 0
	v_mov_b64_e32 v[14:15], 0
	v_mov_b64_e32 v[16:17], 0
	v_mov_b64_e32 v[18:19], 0
	v_mov_b64_e32 v[20:21], 0
	v_mov_b64_e32 v[22:23], 0
	v_mov_b64_e32 v[24:25], 0
	v_mov_b64_e32 v[26:27], 0
	v_mov_b64_e32 v[28:29], 0
	v_mov_b64_e32 v[30:31], 0
	v_mov_b64_e32 v[32:33], 0
	v_mov_b64_e32 v[34:35], 0
	v_mov_b64_e32 v[36:37], 0
	v_mov_b64_e32 v[38:39], 0
	v_mov_b64_e32 v[40:41], 0
	v_mov_b64_e32 v[42:43], 0
	v_mov_b64_e32 v[44:45], 0
	v_mov_b64_e32 v[46:47], 0
	v_mov_b64_e32 v[48:49], 0
	v_mov_b64_e32 v[50:51], 0
	v_mov_b64_e32 v[52:53], 0
	v_mov_b64_e32 v[54:55], 0
	v_mov_b64_e32 v[56:57], 0
	v_mov_b64_e32 v[58:59], 0
	v_mov_b64_e32 v[60:61], 0
	v_mov_b64_e32 v[62:63], 0
	v_mov_b64_e32 v[64:65], 0
	v_mov_b64_e32 v[66:67], 0
	v_mov_b64_e32 v[72:73], 0
	v_mov_b64_e32 v[74:75], 0
	v_mov_b64_e32 v[76:77], 0
	v_mov_b64_e32 v[78:79], 0
	v_mov_b64_e32 v[84:85], 0
	v_mov_b64_e32 v[86:87], 0
	v_mov_b64_e32 v[88:89], 0
	v_mov_b64_e32 v[90:91], 0
	v_mov_b64_e32 v[96:97], 0
	v_mov_b64_e32 v[98:99], 0
	v_mov_b64_e32 v[100:101], 0
	v_mov_b64_e32 v[102:103], 0
	v_mov_b64_e32 v[108:109], 0
	v_mov_b64_e32 v[110:111], 0
	v_mov_b64_e32 v[112:113], 0
	v_mov_b64_e32 v[114:115], 0
	v_mov_b64_e32 v[120:121], 0
	v_mov_b64_e32 v[122:123], 0
	v_mov_b64_e32 v[124:125], 0
	v_mov_b64_e32 v[126:127], 0
	v_mov_b64_e32 v[132:133], 0
	v_mov_b64_e32 v[134:135], 0
	v_mov_b64_e32 v[152:153], 0
	v_mov_b64_e32 v[154:155], 0
	v_mov_b64_e32 v[160:161], 0
	v_mov_b64_e32 v[162:163], 0
	v_mov_b64_e32 v[164:165], 0
	v_mov_b64_e32 v[166:167], 0
	v_mov_b64_e32 v[172:173], 0
	v_mov_b64_e32 v[174:175], 0

.LBB0_1669:
	s_andn2_b64 vcc, exec, s[18:19]
	s_cbranch_vccnz .LBB0_1693
	s_add_u32 s70, s48, 0x100
	s_addc_u32 s71, s49, 0
	s_add_u32 s72, s46, 0x100
	s_addc_u32 s73, s47, 0
	s_add_u32 s74, s44, 0x100
	s_addc_u32 s75, s45, 0
	s_add_u32 s76, s50, 0x100
	v_mov_b32_e32 v0, 0
	s_addc_u32 s77, s51, 0
	s_mov_b32 s44, 0
	s_waitcnt lgkmcnt(0)
	v_mov_b64_e32 v[0:1], 0
	v_mov_b64_e32 v[2:3], 0
	v_mov_b64_e32 v[4:5], 0
	v_mov_b64_e32 v[6:7], 0
	v_mov_b64_e32 v[8:9], 0
	v_mov_b64_e32 v[10:11], 0
	v_mov_b64_e32 v[12:13], 0
	v_mov_b64_e32 v[14:15], 0
	v_mov_b64_e32 v[16:17], 0
	v_mov_b64_e32 v[18:19], 0
	v_mov_b64_e32 v[20:21], 0
	v_mov_b64_e32 v[22:23], 0
	v_mov_b64_e32 v[24:25], 0
	v_mov_b64_e32 v[26:27], 0
	v_mov_b64_e32 v[28:29], 0
	v_mov_b64_e32 v[30:31], 0
	v_mov_b64_e32 v[32:33], 0
	v_mov_b64_e32 v[34:35], 0
	v_mov_b64_e32 v[36:37], 0
	v_mov_b64_e32 v[38:39], 0
	v_mov_b64_e32 v[40:41], 0
	v_mov_b64_e32 v[42:43], 0
	v_mov_b64_e32 v[44:45], 0
	v_mov_b64_e32 v[46:47], 0
	v_mov_b64_e32 v[48:49], 0
	v_mov_b64_e32 v[50:51], 0
	v_mov_b64_e32 v[52:53], 0
	v_mov_b64_e32 v[54:55], 0
	v_mov_b64_e32 v[56:57], 0
	v_mov_b64_e32 v[58:59], 0
	v_mov_b64_e32 v[60:61], 0
	v_mov_b64_e32 v[62:63], 0
	v_mov_b64_e32 v[64:65], 0
	v_mov_b64_e32 v[66:67], 0
	v_mov_b64_e32 v[68:69], 0
	v_mov_b64_e32 v[70:71], 0
	v_mov_b64_e32 v[72:73], 0
	v_mov_b64_e32 v[74:75], 0
	v_mov_b64_e32 v[76:77], 0
	v_mov_b64_e32 v[78:79], 0
	v_mov_b64_e32 v[80:81], 0
	v_mov_b64_e32 v[82:83], 0
	v_mov_b64_e32 v[84:85], 0
	v_mov_b64_e32 v[86:87], 0
	v_mov_b64_e32 v[88:89], 0
	v_mov_b64_e32 v[90:91], 0
	v_mov_b64_e32 v[92:93], 0
	v_mov_b64_e32 v[94:95], 0
	v_mov_b64_e32 v[96:97], 0
	v_mov_b64_e32 v[98:99], 0
	v_mov_b64_e32 v[100:101], 0
	v_mov_b64_e32 v[102:103], 0
	v_mov_b64_e32 v[104:105], 0
	v_mov_b64_e32 v[106:107], 0
	v_mov_b64_e32 v[108:109], 0
	v_mov_b64_e32 v[110:111], 0
	v_mov_b64_e32 v[112:113], 0
	v_mov_b64_e32 v[114:115], 0
	v_mov_b64_e32 v[116:117], 0
	v_mov_b64_e32 v[118:119], 0
	v_mov_b64_e32 v[120:121], 0
	v_mov_b64_e32 v[122:123], 0
	v_mov_b64_e32 v[124:125], 0
	v_mov_b64_e32 v[126:127], 0

.Lgx_skip:
	s_xor_b32 s32, s32, 0x400
	v_mbcnt_lo_u32_b32 v255, -1, 0
	v_mbcnt_hi_u32_b32 v255, -1, v255
	v_lshlrev_b32_e32 v255, 2, v255
	v_lshl_add_u32 v255, v164, 13, v255
	s_lshl_b32 s89, s46, 2
	v_add_u32_e32 v255, s89, v255
	s_mov_b32 m0, s32
	s_nop 0
	global_load_lds_dword v255, s[98:99]
	global_load_lds_dword v255, s[98:99] offset:256
	s_add_i32 m0, s32, 0x200
	s_nop 0
	global_load_lds_dword v255, s[100:101]
	global_load_lds_dword v255, s[100:101] offset:256
	v_mov_b64_e32 v[32:33], 0
	v_mov_b64_e32 v[34:35], 0
	v_mov_b64_e32 v[36:37], 0
	v_mov_b64_e32 v[38:39], 0
	v_mov_b64_e32 v[40:41], 0
	v_mov_b64_e32 v[42:43], 0
	v_mov_b64_e32 v[44:45], 0
	v_mov_b64_e32 v[46:47], 0
	v_mov_b64_e32 v[48:49], 0
	v_mov_b64_e32 v[50:51], 0
	v_mov_b64_e32 v[52:53], 0
	v_mov_b64_e32 v[54:55], 0
	v_mov_b64_e32 v[56:57], 0
	v_mov_b64_e32 v[58:59], 0
	v_mov_b64_e32 v[60:61], 0
	v_mov_b64_e32 v[62:63], 0
	v_mov_b64_e32 v[64:65], 0
	v_mov_b64_e32 v[66:67], 0
	v_mov_b64_e32 v[68:69], 0
	v_mov_b64_e32 v[70:71], 0
	v_mov_b64_e32 v[72:73], 0
	v_mov_b64_e32 v[74:75], 0
	v_mov_b64_e32 v[76:77], 0
	v_mov_b64_e32 v[78:79], 0
	v_mov_b64_e32 v[80:81], 0
	v_mov_b64_e32 v[82:83], 0
	v_mov_b64_e32 v[84:85], 0
	v_mov_b64_e32 v[86:87], 0
	v_mov_b64_e32 v[88:89], 0
	v_mov_b64_e32 v[90:91], 0
	v_mov_b64_e32 v[92:93], 0
	v_mov_b64_e32 v[94:95], 0
	v_mov_b64_e32 v[96:97], 0
	v_mov_b64_e32 v[98:99], 0
	v_mov_b64_e32 v[100:101], 0
	v_mov_b64_e32 v[102:103], 0
	v_mov_b64_e32 v[104:105], 0
	v_mov_b64_e32 v[106:107], 0
	v_mov_b64_e32 v[108:109], 0
	v_mov_b64_e32 v[110:111], 0
	v_mov_b64_e32 v[112:113], 0
	v_mov_b64_e32 v[114:115], 0
	v_mov_b64_e32 v[116:117], 0
	v_mov_b64_e32 v[118:119], 0
	v_mov_b64_e32 v[120:121], 0
	v_mov_b64_e32 v[122:123], 0
	v_mov_b64_e32 v[124:125], 0
	v_mov_b64_e32 v[126:127], 0
	v_mov_b64_e32 v[128:129], 0
	v_mov_b64_e32 v[130:131], 0
	v_mov_b64_e32 v[132:133], 0
	v_mov_b64_e32 v[134:135], 0
	v_mov_b64_e32 v[136:137], 0
	v_mov_b64_e32 v[138:139], 0
	v_mov_b64_e32 v[140:141], 0
	v_mov_b64_e32 v[142:143], 0
	v_mov_b64_e32 v[144:145], 0
	v_mov_b64_e32 v[146:147], 0
	v_mov_b64_e32 v[148:149], 0
	v_mov_b64_e32 v[150:151], 0
	v_mov_b64_e32 v[152:153], 0
	v_mov_b64_e32 v[154:155], 0
	v_mov_b64_e32 v[156:157], 0
	v_mov_b64_e32 v[158:159], 0
	s_branch .LBB0_2279

.LBB0_2281:
	v_mov_b32_e32 v159, 0
	v_mov_b64_e32 v[32:33], 0
	v_mov_b64_e32 v[34:35], 0
	v_mov_b64_e32 v[36:37], 0
	v_mov_b64_e32 v[38:39], 0
	v_mov_b64_e32 v[40:41], 0
	v_mov_b64_e32 v[42:43], 0
	v_mov_b64_e32 v[44:45], 0
	v_mov_b64_e32 v[46:47], 0
	v_mov_b64_e32 v[48:49], 0
	v_mov_b64_e32 v[50:51], 0
	v_mov_b64_e32 v[52:53], 0
	v_mov_b64_e32 v[54:55], 0
	v_mov_b64_e32 v[56:57], 0
	v_mov_b64_e32 v[58:59], 0
	v_mov_b64_e32 v[60:61], 0
	v_mov_b64_e32 v[62:63], 0
	v_mov_b64_e32 v[64:65], 0
	v_mov_b64_e32 v[66:67], 0
	v_mov_b64_e32 v[68:69], 0
	v_mov_b64_e32 v[70:71], 0
	v_mov_b64_e32 v[72:73], 0
	v_mov_b64_e32 v[74:75], 0
	v_mov_b64_e32 v[76:77], 0
	v_mov_b64_e32 v[78:79], 0
	v_mov_b64_e32 v[80:81], 0
	v_mov_b64_e32 v[82:83], 0
	v_mov_b64_e32 v[84:85], 0
	v_mov_b64_e32 v[86:87], 0
	v_mov_b64_e32 v[88:89], 0
	v_mov_b64_e32 v[90:91], 0
	v_mov_b64_e32 v[92:93], 0
	v_mov_b64_e32 v[94:95], 0
	v_mov_b64_e32 v[96:97], 0
	v_mov_b64_e32 v[98:99], 0
	v_mov_b64_e32 v[100:101], 0
	v_mov_b64_e32 v[102:103], 0
	v_mov_b64_e32 v[104:105], 0
	v_mov_b64_e32 v[106:107], 0
	v_mov_b64_e32 v[108:109], 0
	v_mov_b64_e32 v[110:111], 0
	v_mov_b64_e32 v[112:113], 0
	v_mov_b64_e32 v[114:115], 0
	v_mov_b64_e32 v[116:117], 0
	v_mov_b64_e32 v[118:119], 0
	v_mov_b64_e32 v[120:121], 0
	v_mov_b64_e32 v[122:123], 0
	v_mov_b64_e32 v[124:125], 0
	v_mov_b64_e32 v[126:127], 0
	v_mov_b64_e32 v[128:129], 0
	v_mov_b64_e32 v[130:131], 0
	v_mov_b64_e32 v[132:133], 0
	v_mov_b64_e32 v[134:135], 0
	v_mov_b64_e32 v[136:137], 0
	v_mov_b64_e32 v[138:139], 0
	v_mov_b64_e32 v[140:141], 0
	v_mov_b64_e32 v[142:143], 0
	v_mov_b64_e32 v[144:145], 0
	v_mov_b64_e32 v[146:147], 0
	v_mov_b64_e32 v[148:149], 0
	v_mov_b64_e32 v[150:151], 0
	v_mov_b64_e32 v[152:153], 0
	v_mov_b64_e32 v[154:155], 0
	v_mov_b64_e32 v[156:157], 0
	v_mov_b64_e32 v[158:159], 0

.LBB0_2363:
	s_andn2_b64 vcc, exec, s[14:15]
	s_cbranch_vccnz .LBB0_2371
	s_add_u32 s45, s54, 0x100
	s_addc_u32 s47, s55, 0
	s_add_u32 s78, s52, 0x100
	s_addc_u32 s79, s53, 0
	s_add_u32 s80, s48, 0x100
	s_addc_u32 s81, s49, 0
	s_add_u32 s82, s50, 0x100
	v_mov_b32_e32 v24, 0
	s_addc_u32 s83, s51, 0
	s_mov_b32 s48, 0
	v_mov_b64_e32 v[24:25], 0
	v_mov_b64_e32 v[26:27], 0
	v_mov_b64_e32 v[28:29], 0
	v_mov_b64_e32 v[30:31], 0
	v_mov_b64_e32 v[32:33], 0
	v_mov_b64_e32 v[34:35], 0
	v_mov_b64_e32 v[36:37], 0
	v_mov_b64_e32 v[38:39], 0
	v_mov_b64_e32 v[40:41], 0
	v_mov_b64_e32 v[42:43], 0
	v_mov_b64_e32 v[44:45], 0
	v_mov_b64_e32 v[46:47], 0
	v_mov_b64_e32 v[48:49], 0
	v_mov_b64_e32 v[50:51], 0
	v_mov_b64_e32 v[52:53], 0
	v_mov_b64_e32 v[54:55], 0
	v_mov_b64_e32 v[56:57], 0
	v_mov_b64_e32 v[58:59], 0
	v_mov_b64_e32 v[60:61], 0
	v_mov_b64_e32 v[62:63], 0
	v_mov_b64_e32 v[64:65], 0
	v_mov_b64_e32 v[66:67], 0
	v_mov_b64_e32 v[68:69], 0
	v_mov_b64_e32 v[70:71], 0
	v_mov_b64_e32 v[72:73], 0
	v_mov_b64_e32 v[74:75], 0
	v_mov_b64_e32 v[76:77], 0
	v_mov_b64_e32 v[78:79], 0
	v_mov_b64_e32 v[80:81], 0
	v_mov_b64_e32 v[82:83], 0
	v_mov_b64_e32 v[84:85], 0
	v_mov_b64_e32 v[86:87], 0
	v_mov_b64_e32 v[88:89], 0
	v_mov_b64_e32 v[90:91], 0
	v_mov_b64_e32 v[92:93], 0
	v_mov_b64_e32 v[94:95], 0
	v_mov_b64_e32 v[96:97], 0
	v_mov_b64_e32 v[98:99], 0
	v_mov_b64_e32 v[100:101], 0
	v_mov_b64_e32 v[102:103], 0
	v_mov_b64_e32 v[104:105], 0
	v_mov_b64_e32 v[106:107], 0
	v_mov_b64_e32 v[108:109], 0
	v_mov_b64_e32 v[110:111], 0
	v_mov_b64_e32 v[112:113], 0
	v_mov_b64_e32 v[114:115], 0
	v_mov_b64_e32 v[116:117], 0
	v_mov_b64_e32 v[118:119], 0
	v_mov_b64_e32 v[120:121], 0
	v_mov_b64_e32 v[122:123], 0
	v_mov_b64_e32 v[124:125], 0
	v_mov_b64_e32 v[126:127], 0
	v_mov_b64_e32 v[128:129], 0
	v_mov_b64_e32 v[130:131], 0
	v_mov_b64_e32 v[132:133], 0
	v_mov_b64_e32 v[134:135], 0
	v_mov_b64_e32 v[136:137], 0
	v_mov_b64_e32 v[138:139], 0
	v_mov_b64_e32 v[140:141], 0
	v_mov_b64_e32 v[142:143], 0
	v_mov_b64_e32 v[144:145], 0
	v_mov_b64_e32 v[146:147], 0
	v_mov_b64_e32 v[148:149], 0
	v_mov_b64_e32 v[150:151], 0
